# in-proj: next-tile computation reduced to 14 scalar ops (constant shapes) instead of a generic v_rcp division; plus v57 stack
# baseline (speedup 1.0000x reference)
.LBB0_262:
	s_add_i32 s93, s93, 1
	s_mul_i32 s4, s93, s23
	s_mul_hi_u32 s5, s93, s22
	s_add_i32 s5, s5, s4
	s_mul_i32 s4, s93, s22
	s_add_u32 s26, s4, s12
	s_addc_u32 s27, s5, s63
	v_mov_b64_e32 v[4:5], 0x600
	v_cmp_gt_i64_e32 vcc, s[26:27], v[160:161]
	v_cmp_lt_i64_e64 s[4:5], s[26:27], v[4:5]
	s_cbranch_vccnz .LBB0_264
	s_and_b32 s13, s26, 7
	s_lshr_b32 s21, s26, 3
	s_mulk_i32 s13, 0xc0
	s_add_i32 s13, s13, s21
	s_mul_i32 s21, s13, 0x2aab
	s_lshr_b32 s21, s21, 22
	s_mul_i32 s27, s21, 0x180
	s_sub_i32 s13, s13, s27
	s_lshl_b32 s26, s21, 3
	s_and_b32 s27, s13, 7
	s_add_i32 s72, s26, s27
	s_lshr_b32 s21, s13, 3
	s_cmp_lg_u32 s21, 35
	s_cselect_b32 s74, s21, 52
